# ret_out silu: v_exp_f32/v_rcp_f32 form (as the baseline SwiGLU epilogue) replaces libm expf + IEEE division expansions (22 exp, 28 div sites)
# speedup vs baseline: 1.0077x; 1.0020x over previous
.LBB0_1275:
	ds_read_b128 v[30:33], v183
	ds_read_b128 v[26:29], v183 offset:64
	ds_read_b128 v[34:37], v184 offset:18432
	ds_read_b128 v[38:41], v184 offset:18496
	s_lshl_b32 s0, s87, 5
	s_sub_i32 s2, s82, s0
	s_lshr_b32 s0, s86, 24
	s_waitcnt lgkmcnt(1)
	v_mfma_f32_16x16x32_bf16 v[34:37], v[34:37], v[30:33], 0
	s_add_i32 s0, s82, s0
	s_ashr_i32 s0, s0, 8
	s_ashr_i32 s1, s0, 31
	s_waitcnt lgkmcnt(0)
	v_mfma_f32_16x16x32_bf16 v[54:57], v[38:41], v[26:29], v[34:37]
	ds_read_b128 v[38:41], v184 offset:20800
	s_ashr_i32 s3, s2, 31
	s_nop 0
	ds_read_b128 v[34:37], v184 offset:20736
	s_lshl_b64 s[0:1], s[0:1], 12
	s_lshl_b64 s[86:87], s[2:3], 7
	s_add_u32 s0, s0, s86
	s_addc_u32 s1, s1, s87
	s_waitcnt lgkmcnt(0)
	v_mfma_f32_16x16x32_bf16 v[34:37], v[34:37], v[30:33], 0
	s_lshl_b32 s82, s97, 7
	ds_read_b128 v[58:61], v184 offset:34624
	v_mfma_f32_16x16x32_bf16 v[62:65], v[38:41], v[26:29], v[34:37]
	ds_read_b128 v[38:41], v184 offset:23104
	s_nop 3
	ds_read_b128 v[34:37], v184 offset:23040
	s_waitcnt lgkmcnt(0)
	v_mfma_f32_16x16x32_bf16 v[34:37], v[34:37], v[30:33], 0
	v_mfma_f32_16x16x32_bf16 v[66:69], v[38:41], v[26:29], v[34:37]
	ds_read_b128 v[38:41], v184 offset:25408
	s_nop 5
	ds_read_b128 v[34:37], v184 offset:25344
	s_waitcnt lgkmcnt(0)
	v_mfma_f32_16x16x32_bf16 v[34:37], v[34:37], v[30:33], 0
	v_mfma_f32_16x16x32_bf16 v[50:53], v[38:41], v[26:29], v[34:37]
	ds_read_b128 v[38:41], v184 offset:27712
	s_nop 5
	ds_read_b128 v[34:37], v184 offset:27648
	s_waitcnt lgkmcnt(0)
	v_mfma_f32_16x16x32_bf16 v[34:37], v[34:37], v[30:33], 0
	v_mfma_f32_16x16x32_bf16 v[46:49], v[38:41], v[26:29], v[34:37]
	ds_read_b128 v[38:41], v184 offset:30016
	s_nop 5
	ds_read_b128 v[34:37], v184 offset:29952
	s_waitcnt lgkmcnt(0)
	v_mfma_f32_16x16x32_bf16 v[34:37], v[34:37], v[30:33], 0
	v_mfma_f32_16x16x32_bf16 v[42:45], v[38:41], v[26:29], v[34:37]
	ds_read_b128 v[38:41], v184 offset:32320
	s_nop 5
	ds_read_b128 v[34:37], v184 offset:32256
	s_waitcnt lgkmcnt(0)
	v_mfma_f32_16x16x32_bf16 v[34:37], v[34:37], v[30:33], 0
	v_mfma_f32_16x16x32_bf16 v[38:41], v[38:41], v[26:29], v[34:37]
	s_nop 6
	ds_read_b128 v[34:37], v184 offset:34560
	s_waitcnt lgkmcnt(0)
	v_mfma_f32_16x16x32_bf16 v[34:37], v[34:37], v[30:33], 0
	v_mfma_f32_16x16x32_bf16 v[34:37], v[58:61], v[26:29], v[34:37]
	v_mul_f32_e32 v58, v107, v89
	v_mul_f32_e32 v59, v108, v87
	v_cndmask_b32_e64 v58, v59, v58, s[8:9]
	v_mul_f32_e32 v59, v107, v91
	v_mul_f32_e32 v60, v108, v93
	v_cndmask_b32_e64 v59, v59, v60, s[10:11]
	v_mul_f32_e32 v58, 0x3fb8aa3b, v58
	v_mul_f32_e32 v59, 0x3fb8aa3b, v59
	v_exp_f32_e32 v58, v58
	v_exp_f32_e32 v59, v59
	v_mul_f32_e32 v60, v108, v120
	v_pk_mul_f32 v[58:59], v[58:59], v[54:55]
	v_mul_f32_e32 v54, v107, v119
	v_mul_f32_e32 v55, v108, v118
	v_cndmask_b32_e64 v54, v55, v54, s[12:13]
	v_mul_f32_e32 v55, v107, v121
	v_cndmask_b32_e64 v55, v60, v55, s[14:15]
	v_mul_f32_e32 v54, 0x3fb8aa3b, v54
	v_mul_f32_e32 v55, 0x3fb8aa3b, v55
	v_exp_f32_e32 v54, v54
	v_exp_f32_e32 v55, v55
	v_cvt_pk_bf16_f32 v58, v58, v59
	v_pk_mul_f32 v[60:61], v[54:55], v[56:57]
	v_mul_f32_e32 v54, v107, v123
	v_mul_f32_e32 v55, v108, v122
	v_cndmask_b32_e64 v54, v55, v54, s[16:17]
	v_mul_f32_e32 v55, v107, v125
	v_mul_f32_e32 v56, v108, v124
	v_cndmask_b32_e64 v55, v56, v55, s[18:19]
	v_mul_f32_e32 v54, 0x3fb8aa3b, v54
	v_mul_f32_e32 v55, 0x3fb8aa3b, v55
	v_exp_f32_e32 v54, v54
	v_exp_f32_e32 v55, v55
	v_mul_f32_e32 v56, v108, v128
	v_mul_f32_e32 v57, v108, v134
	v_cvt_pk_bf16_f32 v59, v60, v61
	v_pk_mul_f32 v[62:63], v[54:55], v[62:63]
	v_mul_f32_e32 v54, v107, v127
	v_mul_f32_e32 v55, v108, v126
	v_cndmask_b32_e64 v54, v55, v54, s[20:21]
	v_mul_f32_e32 v55, v107, v129
	v_cndmask_b32_e64 v55, v56, v55, s[22:23]
	v_mul_f32_e32 v54, 0x3fb8aa3b, v54
	v_mul_f32_e32 v55, 0x3fb8aa3b, v55
	v_exp_f32_e32 v54, v54
	v_exp_f32_e32 v55, v55
	v_mul_f32_e32 v56, v108, v132
	v_cvt_pk_bf16_f32 v60, v62, v63
	v_pk_mul_f32 v[64:65], v[54:55], v[64:65]
	v_mul_f32_e32 v54, v107, v131
	v_mul_f32_e32 v55, v108, v130
	v_cndmask_b32_e64 v54, v55, v54, s[24:25]
	v_mul_f32_e32 v55, v107, v133
	v_cndmask_b32_e64 v55, v56, v55, s[26:27]
	v_mul_f32_e32 v54, 0x3fb8aa3b, v54
	v_mul_f32_e32 v55, 0x3fb8aa3b, v55
	v_exp_f32_e32 v54, v54
	v_exp_f32_e32 v55, v55
	v_mul_f32_e32 v56, v107, v135
	v_cndmask_b32_e64 v56, v57, v56, s[28:29]
	v_mul_f32_e32 v57, v107, v137
	v_pk_mul_f32 v[54:55], v[54:55], v[66:67]
	v_mul_f32_e32 v66, v108, v136
	v_cndmask_b32_e64 v57, v66, v57, s[30:31]
	v_mul_f32_e32 v56, 0x3fb8aa3b, v56
	v_mul_f32_e32 v57, 0x3fb8aa3b, v57
	v_exp_f32_e32 v56, v56
	v_exp_f32_e32 v57, v57
	v_mul_f32_e32 v66, v107, v139
	v_mul_f32_e32 v67, v108, v138
	v_cndmask_b32_e64 v66, v67, v66, s[34:35]
	v_pk_mul_f32 v[56:57], v[56:57], v[68:69]
	v_mul_f32_e32 v67, v107, v141
	v_mul_f32_e32 v68, v108, v140
	v_cndmask_b32_e64 v67, v68, v67, s[36:37]
	v_mul_f32_e32 v66, 0x3fb8aa3b, v66
	v_mul_f32_e32 v67, 0x3fb8aa3b, v67
	v_exp_f32_e32 v66, v66
	v_exp_f32_e32 v67, v67
	v_mul_f32_e32 v68, v108, v144
	v_cvt_pk_bf16_f32 v61, v64, v65
	v_cvt_pk_bf16_f32 v54, v54, v55
	v_pk_mul_f32 v[50:51], v[66:67], v[50:51]
	v_mul_f32_e32 v66, v107, v143
	v_mul_f32_e32 v67, v108, v142
	v_cndmask_b32_e64 v66, v67, v66, s[38:39]
	v_mul_f32_e32 v67, v107, v145
	v_cndmask_b32_e64 v67, v68, v67, s[40:41]
	v_mul_f32_e32 v66, 0x3fb8aa3b, v66
	v_mul_f32_e32 v67, 0x3fb8aa3b, v67
	v_exp_f32_e32 v66, v66
	v_exp_f32_e32 v67, v67
	v_mul_f32_e32 v68, v108, v148
	v_cvt_pk_bf16_f32 v55, v56, v57
	v_cvt_pk_bf16_f32 v56, v50, v51
	v_pk_mul_f32 v[52:53], v[66:67], v[52:53]
	v_mul_f32_e32 v66, v107, v147
	v_mul_f32_e32 v67, v108, v146
	v_cndmask_b32_e64 v66, v67, v66, s[42:43]
	v_mul_f32_e32 v67, v107, v149
	v_cndmask_b32_e64 v67, v68, v67, s[44:45]
	v_mul_f32_e32 v66, 0x3fb8aa3b, v66
	v_mul_f32_e32 v67, 0x3fb8aa3b, v67
	v_exp_f32_e32 v66, v66
	v_exp_f32_e32 v67, v67
	v_mul_f32_e32 v68, v108, v152
	v_cvt_pk_bf16_f32 v57, v52, v53
	v_pk_mul_f32 v[46:47], v[66:67], v[46:47]
	v_mul_f32_e32 v66, v107, v151
	v_mul_f32_e32 v67, v108, v150
	v_cndmask_b32_e64 v66, v67, v66, s[46:47]
	v_mul_f32_e32 v67, v107, v153
	v_cndmask_b32_e64 v67, v68, v67, s[48:49]
	v_mul_f32_e32 v66, 0x3fb8aa3b, v66
	v_mul_f32_e32 v67, 0x3fb8aa3b, v67
	v_exp_f32_e32 v66, v66
	v_exp_f32_e32 v67, v67
	v_mul_f32_e32 v68, v108, v156
	v_cvt_pk_bf16_f32 v46, v46, v47
	v_pk_mul_f32 v[48:49], v[66:67], v[48:49]
	v_mul_f32_e32 v66, v107, v155
	v_mul_f32_e32 v67, v108, v154
	v_cndmask_b32_e64 v66, v67, v66, s[50:51]
	v_mul_f32_e32 v67, v107, v157
	v_cndmask_b32_e64 v67, v68, v67, s[52:53]
	v_mul_f32_e32 v66, 0x3fb8aa3b, v66
	v_mul_f32_e32 v67, 0x3fb8aa3b, v67
	v_exp_f32_e32 v66, v66
	v_exp_f32_e32 v67, v67
	v_mul_f32_e32 v68, v108, v160
	v_cvt_pk_bf16_f32 v47, v48, v49
	v_pk_mul_f32 v[42:43], v[66:67], v[42:43]
	v_mul_f32_e32 v66, v107, v159
	v_mul_f32_e32 v67, v108, v158
	v_cndmask_b32_e64 v66, v67, v66, s[54:55]
	v_mul_f32_e32 v67, v107, v161
	v_cndmask_b32_e64 v67, v68, v67, s[94:95]
	v_mul_f32_e32 v66, 0x3fb8aa3b, v66
	v_mul_f32_e32 v67, 0x3fb8aa3b, v67
	v_exp_f32_e32 v66, v66
	v_exp_f32_e32 v67, v67
	v_mul_f32_e32 v68, v108, v164
	v_cvt_pk_bf16_f32 v48, v42, v43
	v_pk_mul_f32 v[44:45], v[66:67], v[44:45]
	v_mul_f32_e32 v66, v107, v163
	v_mul_f32_e32 v67, v108, v162
	v_cndmask_b32_e64 v66, v67, v66, s[58:59]
	v_mul_f32_e32 v67, v107, v165
	v_cndmask_b32_e64 v67, v68, v67, s[60:61]
	v_mul_f32_e32 v66, 0x3fb8aa3b, v66
	v_mul_f32_e32 v67, 0x3fb8aa3b, v67
	v_exp_f32_e32 v66, v66
	v_exp_f32_e32 v67, v67
	v_mul_f32_e32 v68, v108, v168
	v_cvt_pk_bf16_f32 v49, v44, v45
	v_pk_mul_f32 v[38:39], v[66:67], v[38:39]
	v_mul_f32_e32 v66, v107, v167
	v_mul_f32_e32 v67, v108, v166
	v_cndmask_b32_e64 v66, v67, v66, s[62:63]
	v_mul_f32_e32 v67, v107, v169
	v_cndmask_b32_e64 v67, v68, v67, s[64:65]
	v_mul_f32_e32 v66, 0x3fb8aa3b, v66
	v_mul_f32_e32 v67, 0x3fb8aa3b, v67
	v_exp_f32_e32 v66, v66
	v_exp_f32_e32 v67, v67
	v_mul_f32_e32 v68, v108, v172
	v_cvt_pk_bf16_f32 v38, v38, v39
	v_pk_mul_f32 v[40:41], v[66:67], v[40:41]
	v_mul_f32_e32 v66, v107, v171
	v_mul_f32_e32 v67, v108, v170
	v_cndmask_b32_e64 v66, v67, v66, s[66:67]
	v_mul_f32_e32 v67, v107, v173
	v_cndmask_b32_e64 v67, v68, v67, s[68:69]
	v_mul_f32_e32 v66, 0x3fb8aa3b, v66
	v_mul_f32_e32 v67, 0x3fb8aa3b, v67
	v_exp_f32_e32 v66, v66
	v_exp_f32_e32 v67, v67
	v_mul_f32_e32 v68, v108, v176
	v_cvt_pk_bf16_f32 v39, v40, v41
	v_pk_mul_f32 v[34:35], v[66:67], v[34:35]
	v_mul_f32_e32 v66, v107, v175
	v_mul_f32_e32 v67, v108, v174
	v_cndmask_b32_e64 v66, v67, v66, s[70:71]
	v_mul_f32_e32 v67, v107, v177
	v_cndmask_b32_e64 v67, v68, v67, s[72:73]
	v_mul_f32_e32 v66, 0x3fb8aa3b, v66
	v_mul_f32_e32 v67, 0x3fb8aa3b, v67
	v_exp_f32_e32 v66, v66
	v_exp_f32_e32 v67, v67
	v_cvt_pk_bf16_f32 v40, v34, v35
	v_pk_mul_f32 v[36:37], v[66:67], v[36:37]
	ds_read_b64_tr_b16 v[64:65], v185 offset:39168
	ds_read_b64_tr_b16 v[62:63], v185 offset:36864
	ds_read_b64_tr_b16 v[66:67], v185 offset:36896
	ds_read_b64_tr_b16 v[68:69], v185 offset:39200
	ds_read_b64_tr_b16 v[110:111], v185 offset:36928
	ds_read_b64_tr_b16 v[112:113], v185 offset:39232
	ds_read_b64_tr_b16 v[192:193], v185 offset:36960
	ds_read_b64_tr_b16 v[194:195], v185 offset:39264
	s_waitcnt lgkmcnt(6)
	v_mfma_f32_16x16x32_bf16 v[62:65], v[62:65], v[58:61], 0
	v_cvt_pk_bf16_f32 v41, v36, v37
	s_waitcnt lgkmcnt(4)
	v_mfma_f32_16x16x32_bf16 v[66:69], v[66:69], v[58:61], 0
	s_waitcnt lgkmcnt(2)
	v_mfma_f32_16x16x32_bf16 v[110:113], v[110:113], v[58:61], 0
	s_waitcnt lgkmcnt(0)
	v_mfma_f32_16x16x32_bf16 v[58:61], v[192:195], v[58:61], 0
	ds_read_b64_tr_b16 v[52:53], v186 offset:39168
	ds_read_b64_tr_b16 v[50:51], v186 offset:36864
	ds_read_b64_tr_b16 v[192:193], v186 offset:36896
	ds_read_b64_tr_b16 v[194:195], v186 offset:39200
	s_waitcnt lgkmcnt(2)
	v_mfma_f32_16x16x32_bf16 v[50:53], v[50:53], v[54:57], v[62:65]
	s_waitcnt lgkmcnt(0)
	v_mfma_f32_16x16x32_bf16 v[62:65], v[192:195], v[54:57], v[66:69]
	s_nop 2
	ds_read_b64_tr_b16 v[66:67], v186 offset:36928
	ds_read_b64_tr_b16 v[68:69], v186 offset:39232
	s_waitcnt lgkmcnt(0)
	v_mfma_f32_16x16x32_bf16 v[66:69], v[66:69], v[54:57], v[110:113]
	s_nop 2
	ds_read_b64_tr_b16 v[110:111], v186 offset:36960
	ds_read_b64_tr_b16 v[112:113], v186 offset:39264
	s_waitcnt lgkmcnt(0)
	v_mfma_f32_16x16x32_bf16 v[54:57], v[110:113], v[54:57], v[58:61]
	ds_read_b64_tr_b16 v[44:45], v187 offset:39168
	ds_read_b64_tr_b16 v[42:43], v187 offset:36864
	s_nop 0
	ds_read_b64_tr_b16 v[58:59], v187 offset:36896
	ds_read_b64_tr_b16 v[60:61], v187 offset:39200
	s_waitcnt lgkmcnt(2)
	v_mfma_f32_16x16x32_bf16 v[42:45], v[42:45], v[46:49], v[50:53]
	s_nop 2
	ds_read_b64_tr_b16 v[50:51], v187 offset:36928
	ds_read_b64_tr_b16 v[52:53], v187 offset:39232
	s_waitcnt lgkmcnt(2)
	v_mfma_f32_16x16x32_bf16 v[58:61], v[58:61], v[46:49], v[62:65]
	s_waitcnt lgkmcnt(0)
	v_mfma_f32_16x16x32_bf16 v[62:65], v[50:53], v[46:49], v[66:69]
	ds_read_b64_tr_b16 v[50:51], v187 offset:36960
	ds_read_b64_tr_b16 v[52:53], v187 offset:39264
	s_waitcnt lgkmcnt(0)
	v_mfma_f32_16x16x32_bf16 v[54:57], v[50:53], v[46:49], v[54:57]
	ds_read_b64_tr_b16 v[36:37], v188 offset:39168
	ds_read_b64_tr_b16 v[34:35], v188 offset:36864
	ds_read_b64_tr_b16 v[46:47], v188 offset:36896
	ds_read_b64_tr_b16 v[48:49], v188 offset:39200
	s_waitcnt lgkmcnt(2)
	v_mfma_f32_16x16x32_bf16 v[50:53], v[34:37], v[38:41], v[42:45]
	s_nop 2
	ds_read_b64_tr_b16 v[42:43], v188 offset:36928
	ds_read_b64_tr_b16 v[44:45], v188 offset:39232
	s_waitcnt lgkmcnt(2)
	v_mfma_f32_16x16x32_bf16 v[34:37], v[46:49], v[38:41], v[58:61]
	s_waitcnt lgkmcnt(0)
	v_mfma_f32_16x16x32_bf16 v[46:49], v[42:45], v[38:41], v[62:65]
	ds_read_b64_tr_b16 v[42:43], v188 offset:36960
	ds_read_b64_tr_b16 v[44:45], v188 offset:39264
	ds_read_b128 v[110:113], v178 offset:59968
	ds_read_b128 v[62:65], v178 offset:57664
	s_waitcnt lgkmcnt(2)
	v_mfma_f32_16x16x32_bf16 v[192:195], v[42:45], v[38:41], v[54:57]
	ds_read_b128 v[38:41], v178 offset:55296
	s_nop 1
	ds_read_b128 v[54:57], v178 offset:55360
	ds_read_b128 v[42:45], v178 offset:64512
	s_waitcnt lgkmcnt(2)
	v_mfma_f32_16x16x32_bf16 v[38:41], v[38:41], v[30:33], 0
	ds_read_b128 v[66:69], v180 offset:64512
	ds_read_b128 v[196:199], v181 offset:64512
	s_waitcnt lgkmcnt(3)
	v_mfma_f32_16x16x32_bf16 v[54:57], v[54:57], v[26:29], v[38:41]
	s_nop 3
	ds_read_b128 v[38:41], v178 offset:64576
	s_waitcnt lgkmcnt(3)
	v_mfma_f32_16x16x32_bf16 v[42:45], v[42:45], v[30:33], 0
	s_waitcnt lgkmcnt(0)
	v_mfma_f32_16x16x32_bf16 v[58:61], v[38:41], v[26:29], v[42:45]
	ds_read_b128 v[38:41], v178 offset:57600
	s_nop 4
	ds_read_b128 v[42:45], v179 offset:64512
	s_waitcnt lgkmcnt(1)
	v_mfma_f32_16x16x32_bf16 v[38:41], v[38:41], v[30:33], 0
	v_mfma_f32_16x16x32_bf16 v[38:41], v[62:65], v[26:29], v[38:41]
	ds_read_b128 v[62:65], v179 offset:64576
	s_waitcnt lgkmcnt(1)
	v_mfma_f32_16x16x32_bf16 v[42:45], v[42:45], v[30:33], 0
	s_waitcnt lgkmcnt(0)
	v_mfma_f32_16x16x32_bf16 v[42:45], v[62:65], v[26:29], v[42:45]
	ds_read_b128 v[62:65], v178 offset:59904
	s_waitcnt lgkmcnt(0)
	v_mfma_f32_16x16x32_bf16 v[62:65], v[62:65], v[30:33], 0
	v_mfma_f32_16x16x32_bf16 v[62:65], v[110:113], v[26:29], v[62:65]
	ds_read_b128 v[110:113], v180 offset:64576
	v_mfma_f32_16x16x32_bf16 v[66:69], v[66:69], v[30:33], 0
	s_waitcnt lgkmcnt(0)
	v_mfma_f32_16x16x32_bf16 v[66:69], v[110:113], v[26:29], v[66:69]
	ds_read_b128 v[110:113], v178 offset:62208
	s_waitcnt lgkmcnt(0)
	v_mfma_f32_16x16x32_bf16 v[110:113], v[110:113], v[30:33], 0
	v_mfma_f32_16x16x32_bf16 v[30:33], v[196:199], v[30:33], 0
	ds_read_b128 v[196:199], v178 offset:62272
	s_waitcnt lgkmcnt(0)
	v_mfma_f32_16x16x32_bf16 v[196:199], v[196:199], v[26:29], v[110:113]
	s_nop 3
	ds_read_b128 v[110:113], v181 offset:64576
	s_waitcnt lgkmcnt(0)
	v_mfma_f32_16x16x32_bf16 v[26:29], v[110:113], v[26:29], v[30:33]
	s_nop 2
	v_mul_f32_e32 v30, v108, v1
	v_mul_f32_e32 v30, 0x3fb8aa3b, v30
	v_exp_f32_e32 v110, v30
	v_mul_f32_e32 v30, v107, v71
	v_mul_f32_e32 v30, 0x3fb8aa3b, v30
	v_exp_f32_e32 v112, v30
	s_nop 0
	v_pk_mul_f32 v[26:27], v[112:113], v[26:27] op_sel_hi:[0,1]
	v_pk_fma_f32 v[26:27], v[110:111], v[196:197], v[26:27] op_sel_hi:[0,1,1]
	v_pk_add_f32 v[32:33], v[192:193], v[26:27]
	v_pk_mul_f32 v[26:27], v[112:113], v[28:29] op_sel_hi:[0,1]
	v_pk_fma_f32 v[26:27], v[110:111], v[198:199], v[26:27] op_sel_hi:[0,1,1]
	v_pk_add_f32 v[108:109], v[194:195], v[26:27]
	v_lshl_add_u64 v[26:27], s[0:1], 0, v[82:83]
	v_mov_b64_e32 v[28:29], s[80:81]
	v_mad_u64_u32 v[28:29], s[0:1], v26, s90, v[28:29]
	v_pk_mul_f32 v[30:31], v[112:113], v[66:67] op_sel_hi:[0,1]
	v_mad_i32_i24 v29, v27, s90, v29
	v_lshlrev_b64 v[26:27], 12, v[26:27]
	v_pk_fma_f32 v[30:31], v[110:111], v[62:63], v[30:31] op_sel_hi:[0,1,1]
	v_lshl_add_u64 v[28:29], v[28:29], 0, s[82:83]
	v_lshl_add_u64 v[26:27], s[92:93], 0, v[26:27]
	v_pk_add_f32 v[66:67], v[46:47], v[30:31]
	v_lshl_add_u64 v[46:47], v[28:29], 0, v[72:73]
	v_lshl_add_u64 v[26:27], v[26:27], 0, s[82:83]
	s_lshl_b32 s82, s97, 8
	v_lshl_add_u64 v[30:31], v[26:27], 0, v[72:73]
	v_lshl_add_u64 v[62:63], v[84:85], 0, s[82:83]
	global_load_dwordx2 v[114:115], v[46:47], off offset:3072
	global_load_dwordx4 v[26:29], v[62:63], off
	v_pk_mul_f32 v[60:61], v[112:113], v[60:61] op_sel_hi:[0,1]
	v_pk_fma_f32 v[56:57], v[110:111], v[56:57], v[60:61] op_sel_hi:[0,1,1]
	v_pk_add_f32 v[52:53], v[52:53], v[56:57]
	v_pk_mul_f32 v[56:57], v[112:113], v[58:59] op_sel_hi:[0,1]
	v_pk_fma_f32 v[54:55], v[110:111], v[54:55], v[56:57] op_sel_hi:[0,1,1]
	v_pk_add_f32 v[54:55], v[50:51], v[54:55]
	v_pk_mul_f32 v[44:45], v[112:113], v[44:45] op_sel_hi:[0,1]
	v_add_f32_e32 v50, 0, v54
	v_add_f32_e32 v56, v55, v50
	v_add_f32_e32 v56, v52, v56
	s_mov_b32 s82, s96
	s_waitcnt vmcnt(1)
	v_lshlrev_b32_e32 v57, 16, v114
	v_and_b32_e32 v58, 0xffff0000, v114
	v_lshlrev_b32_e32 v60, 16, v115
	v_and_b32_e32 v61, 0xffff0000, v115
	v_mul_f32_e32 v50, 0xbfb8aa3b, v57
	v_exp_f32_e32 v50, v50
	s_nop 0
	v_mul_f32_e32 v51, 0xbfb8aa3b, v58
	v_exp_f32_e32 v51, v51
	s_nop 0
	v_pk_add_f32 v[50:51], v[50:51], 1.0 op_sel_hi:[1,0]
	s_nop 0
	v_rcp_f32_e32 v59, v51
	s_nop 3
	v_mul_f32_e32 v51, v58, v59
	s_nop 1
	v_div_scale_f32 v58, s[0:1], v50, v50, v57
	v_rcp_f32_e32 v59, v58
	v_pk_fma_f32 v[40:41], v[110:111], v[40:41], v[44:45] op_sel_hi:[0,1,1]
	v_pk_add_f32 v[36:37], v[36:37], v[40:41]
	v_pk_mul_f32 v[40:41], v[112:113], v[42:43] op_sel_hi:[0,1]
	v_fma_f32 v103, -v58, v59, 1.0
	v_fmac_f32_e32 v59, v103, v59
	v_div_scale_f32 v103, vcc, v57, v50, v57
	v_mul_f32_e32 v105, v103, v59
	v_fma_f32 v107, -v58, v105, v103
	v_fmac_f32_e32 v105, v107, v59
	v_fma_f32 v58, -v58, v105, v103
	v_div_fmas_f32 v58, v58, v59, v105
	v_div_fixup_f32 v50, v58, v50, v57
	v_add_f32_e32 v58, v53, v56
	v_pk_mul_f32 v[56:57], v[112:113], v[68:69] op_sel_hi:[0,1]
	v_pk_fma_f32 v[56:57], v[110:111], v[64:65], v[56:57] op_sel_hi:[0,1,1]
	v_pk_add_f32 v[56:57], v[48:49], v[56:57]
	v_pk_fma_f32 v[38:39], v[110:111], v[38:39], v[40:41] op_sel_hi:[0,1,1]
	v_pk_add_f32 v[34:35], v[34:35], v[38:39]
	v_add_f32_e32 v38, v58, v34
	v_mul_f32_e32 v48, 0xbfb8aa3b, v60
	v_exp_f32_e32 v48, v48
	s_nop 0
	v_add_f32_e32 v42, v35, v38
	v_mul_f32_e32 v49, 0xbfb8aa3b, v61
	v_exp_f32_e32 v49, v49
	s_nop 0
	v_pk_add_f32 v[48:49], v[48:49], 1.0 op_sel_hi:[1,0]
	s_nop 0
	v_rcp_f32_e32 v59, v49
	s_nop 3
	v_mul_f32_e32 v49, v61, v59
	s_nop 1
	v_rcp_f32_e32 v59, v48
	s_nop 3
	v_mul_f32_e32 v48, v60, v59
	s_nop 1
	global_load_dwordx2 v[60:61], v[46:47], off offset:3104
	s_waitcnt vmcnt(0)
	v_lshlrev_b32_e32 v40, 16, v60
	v_and_b32_e32 v41, 0xffff0000, v60
	v_lshlrev_b32_e32 v65, 16, v61
	v_and_b32_e32 v103, 0xffff0000, v61
	v_mul_f32_e32 v38, 0xbfb8aa3b, v40
	v_exp_f32_e32 v38, v38
	s_nop 0
	v_mul_f32_e32 v39, 0xbfb8aa3b, v41
	v_exp_f32_e32 v39, v39
	s_nop 0
	v_pk_add_f32 v[38:39], v[38:39], 1.0 op_sel_hi:[1,0]
	s_nop 0
	v_rcp_f32_e32 v43, v39
	s_nop 3
	v_mul_f32_e32 v41, v41, v43
	s_nop 1
	v_rcp_f32_e32 v39, v38
	s_nop 3
	v_mul_f32_e32 v40, v40, v39
	s_nop 1
	v_add_f32_e32 v38, v36, v42
	v_add_f32_e32 v38, v37, v38
	v_add_f32_e32 v38, v38, v66
	v_add_f32_e32 v38, v67, v38
	v_add_f32_e32 v38, v56, v38
	v_add_f32_e32 v38, v57, v38
	v_add_f32_e32 v38, v38, v32
	v_add_f32_e32 v38, v33, v38
	v_add_f32_e32 v38, v108, v38
	v_add_f32_e32 v38, v109, v38
	ds_bpermute_b32 v39, v116, v38
	v_cmp_nlt_f32_e32 vcc, s89, v65
	s_waitcnt lgkmcnt(0)
	v_add_f32_e32 v38, v38, v39
	ds_bpermute_b32 v39, v117, v38
	s_waitcnt lgkmcnt(0)
	v_add_f32_e32 v38, v38, v39
	v_mul_f32_e32 v64, 0x3c800000, v38
	v_pk_add_f32 v[38:39], v[56:57], v[64:65] op_sel_hi:[1,0] neg_lo:[0,1] neg_hi:[0,1]
	v_mul_f32_e32 v56, 0xbfb8aa3b, v65
	v_fma_f32 v57, v65, s91, -v56
	v_rndne_f32_e32 v105, v56
	v_fmac_f32_e32 v57, 0xb2a5705f, v65
	v_sub_f32_e32 v56, v56, v105
	v_add_f32_e32 v56, v56, v57
	v_exp_f32_e32 v56, v56
	v_cvt_i32_f32_e32 v57, v105
	v_pk_add_f32 v[44:45], v[34:35], v[64:65] op_sel_hi:[1,0] neg_lo:[0,1] neg_hi:[0,1]
	v_pk_add_f32 v[34:35], v[32:33], v[64:65] op_sel_hi:[1,0] neg_lo:[0,1] neg_hi:[0,1]
	v_pk_add_f32 v[32:33], v[108:109], v[64:65] op_sel_hi:[1,0] neg_lo:[0,1] neg_hi:[0,1]
	v_ldexp_f32 v56, v56, v57
	v_cndmask_b32_e32 v56, 0, v56, vcc
	v_cmp_ngt_f32_e32 vcc, s88, v65
	s_nop 1
	v_pk_add_f32 v[54:55], v[54:55], v[64:65] op_sel_hi:[1,0] neg_lo:[0,1] neg_hi:[0,1]
	v_cndmask_b32_e32 v56, v191, v56, vcc
	v_pk_mul_f32 v[68:69], v[54:55], v[54:55]
	v_pk_add_f32 v[52:53], v[52:53], v[64:65] op_sel_hi:[1,0] neg_lo:[0,1] neg_hi:[0,1]
	v_pk_mul_f32 v[110:111], v[52:53], v[52:53]
	v_add_f32_e32 v68, v68, v69
	v_mul_f32_e32 v57, 0xbfb8aa3b, v103
	v_exp_f32_e32 v57, v57
	s_nop 0
	v_pk_add_f32 v[56:57], v[56:57], 1.0 op_sel_hi:[1,0]
	v_add_f32_e32 v68, v110, v68
	v_div_scale_f32 v105, s[0:1], v57, v57, v103
	v_rcp_f32_e32 v107, v105
	v_pk_mul_f32 v[112:113], v[44:45], v[44:45]
	v_add_f32_e32 v68, v111, v68
	v_pk_add_f32 v[42:43], v[36:37], v[64:65] op_sel_hi:[1,0] neg_lo:[0,1] neg_hi:[0,1]
	v_fma_f32 v108, -v105, v107, 1.0
	v_fmac_f32_e32 v107, v108, v107
	v_div_scale_f32 v108, vcc, v103, v57, v103
	v_mul_f32_e32 v109, v108, v107
	v_fma_f32 v192, -v105, v109, v108
	v_fmac_f32_e32 v109, v192, v107
	v_fma_f32 v105, -v105, v109, v108
	v_div_fmas_f32 v105, v105, v107, v109
	v_div_fixup_f32 v57, v105, v57, v103
	v_div_scale_f32 v103, s[0:1], v56, v56, v65
	v_rcp_f32_e32 v105, v103
	v_add_f32_e32 v68, v112, v68
	v_pk_mul_f32 v[114:115], v[42:43], v[42:43]
	v_add_f32_e32 v68, v113, v68
	v_fma_f32 v107, -v103, v105, 1.0
	v_fmac_f32_e32 v105, v107, v105
	v_div_scale_f32 v107, vcc, v65, v56, v65
	v_mul_f32_e32 v108, v107, v105
	v_fma_f32 v109, -v103, v108, v107
	v_fmac_f32_e32 v108, v109, v105
	v_fma_f32 v103, -v103, v108, v107
	v_div_fmas_f32 v103, v103, v105, v108
	v_div_fixup_f32 v56, v103, v56, v65
	v_pk_add_f32 v[64:65], v[66:67], v[64:65] op_sel_hi:[1,0] neg_lo:[0,1] neg_hi:[0,1]
	v_add_f32_e32 v68, v114, v68
	v_pk_mul_f32 v[66:67], v[64:65], v[64:65]
	v_add_f32_e32 v68, v115, v68
	v_add_f32_e32 v66, v66, v68
	v_pk_mul_f32 v[36:37], v[38:39], v[38:39]
	v_add_f32_e32 v66, v67, v66
	v_add_f32_e32 v36, v36, v66
	v_pk_mul_f32 v[58:59], v[34:35], v[34:35]
	v_add_f32_e32 v36, v37, v36
	v_add_f32_e32 v36, v58, v36
	v_pk_mul_f32 v[60:61], v[32:33], v[32:33]
	v_add_f32_e32 v36, v59, v36
	v_add_f32_e32 v36, v60, v36
	v_add_f32_e32 v36, v61, v36
	ds_bpermute_b32 v37, v116, v36
	s_mov_b32 s0, 0xf800000
	global_load_dwordx2 v[108:109], v[46:47], off offset:3136
	s_waitcnt lgkmcnt(0)
	v_add_f32_e32 v36, v36, v37
	ds_bpermute_b32 v37, v117, v36
	s_waitcnt lgkmcnt(0)
	v_add_f32_e32 v36, v36, v37
	v_fmamk_f32 v36, v36, 0x3c800000, v189
	v_cmp_gt_f32_e32 vcc, s0, v36
	v_mul_f32_e32 v37, 0x4f800000, v36
	s_nop 0
	v_cndmask_b32_e32 v36, v36, v37, vcc
	v_sqrt_f32_e32 v37, v36
	s_nop 0
	v_add_u32_e32 v58, -1, v37
	v_fma_f32 v59, -v58, v37, v36
	v_cmp_ge_f32_e64 s[0:1], 0, v59
	v_add_u32_e32 v59, 1, v37
	s_nop 0
	v_cndmask_b32_e64 v58, v37, v58, s[0:1]
	v_fma_f32 v37, -v59, v37, v36
	v_cmp_lt_f32_e64 s[0:1], 0, v37
	s_nop 1
	v_cndmask_b32_e64 v37, v58, v59, s[0:1]
	v_mul_f32_e32 v58, 0x37800000, v37
	v_cndmask_b32_e32 v37, v37, v58, vcc
	v_cmp_class_f32_e32 vcc, v36, v190
	s_nop 1
	v_cndmask_b32_e32 v36, v37, v36, vcc
	v_rcp_f32_e32 v36, v36
	s_nop 3
	v_pk_mul_f32 v[54:55], v[54:55], v[36:37] op_sel_hi:[1,0]
	v_pk_mul_f32 v[44:45], v[44:45], v[36:37] op_sel_hi:[1,0]
	v_pk_mul_f32 v[26:27], v[26:27], v[54:55]
	s_nop 0
	v_pk_mul_f32 v[26:27], v[50:51], v[26:27]
	v_pk_mul_f32 v[50:51], v[52:53], v[36:37] op_sel_hi:[1,0]
	v_cvt_pk_bf16_f32 v26, v26, v27
	v_pk_mul_f32 v[28:29], v[28:29], v[50:51]
	s_nop 0
	v_pk_mul_f32 v[28:29], v[48:49], v[28:29]
	s_nop 0
	v_cvt_pk_bf16_f32 v27, v28, v29
	global_store_dwordx2 v[30:31], v[26:27], off
	global_load_dwordx4 v[26:29], v[62:63], off offset:64
	s_waitcnt vmcnt(0)
	v_pk_mul_f32 v[26:27], v[26:27], v[44:45]
	s_nop 0
	v_pk_mul_f32 v[26:27], v[40:41], v[26:27]
	v_pk_mul_f32 v[40:41], v[42:43], v[36:37] op_sel_hi:[1,0]
	v_cvt_pk_bf16_f32 v26, v26, v27
	v_pk_mul_f32 v[28:29], v[28:29], v[40:41]
	v_lshlrev_b32_e32 v37, 16, v108
	v_pk_mul_f32 v[28:29], v[56:57], v[28:29]
	v_mul_f32_e32 v40, 0xbfb8aa3b, v37
	v_cvt_pk_bf16_f32 v27, v28, v29
	global_store_dwordx2 v[30:31], v[26:27], off offset:32
	global_load_dwordx4 v[26:29], v[62:63], off offset:128
	v_fma_f32 v41, v37, s91, -v40
	v_rndne_f32_e32 v43, v40
	v_fmac_f32_e32 v41, 0xb2a5705f, v37
	v_sub_f32_e32 v40, v40, v43
	v_add_f32_e32 v40, v40, v41
	v_exp_f32_e32 v40, v40
	v_cvt_i32_f32_e32 v41, v43
	v_and_b32_e32 v42, 0xffff0000, v108
	v_cmp_nlt_f32_e32 vcc, s89, v37
	v_ldexp_f32 v40, v40, v41
	v_cndmask_b32_e32 v40, 0, v40, vcc
	v_cmp_ngt_f32_e32 vcc, s88, v37
	s_nop 1
	v_cndmask_b32_e32 v40, v191, v40, vcc
	v_mul_f32_e32 v41, 0xbfb8aa3b, v42
	v_exp_f32_e32 v41, v41
	s_nop 0
	v_pk_add_f32 v[40:41], v[40:41], 1.0 op_sel_hi:[1,0]
	s_nop 0
	v_rcp_f32_e32 v43, v41
	s_nop 3
	v_mul_f32_e32 v41, v42, v43
	s_nop 1
	v_rcp_f32_e32 v42, v40
	s_nop 3
	v_mul_f32_e32 v40, v37, v42
	s_nop 1
	v_pk_mul_f32 v[42:43], v[64:65], v[36:37] op_sel_hi:[1,0]
	v_lshlrev_b32_e32 v37, 16, v109
	v_cmp_nlt_f32_e32 vcc, s89, v37
	v_pk_mul_f32 v[38:39], v[38:39], v[36:37] op_sel_hi:[1,0]
	s_waitcnt vmcnt(0)
	v_pk_mul_f32 v[26:27], v[26:27], v[42:43]
	s_nop 0
	v_pk_mul_f32 v[26:27], v[40:41], v[26:27]
	v_mul_f32_e32 v40, 0xbfb8aa3b, v37
	v_fma_f32 v41, v37, s91, -v40
	v_rndne_f32_e32 v43, v40
	v_fmac_f32_e32 v41, 0xb2a5705f, v37
	v_sub_f32_e32 v40, v40, v43
	v_add_f32_e32 v40, v40, v41
	v_exp_f32_e32 v40, v40
	v_cvt_i32_f32_e32 v41, v43
	v_and_b32_e32 v42, 0xffff0000, v109
	v_pk_mul_f32 v[28:29], v[28:29], v[38:39]
	v_cvt_pk_bf16_f32 v26, v26, v27
	v_ldexp_f32 v40, v40, v41
	v_cndmask_b32_e32 v40, 0, v40, vcc
	v_cmp_ngt_f32_e32 vcc, s88, v37
	s_nop 1
	v_cndmask_b32_e32 v40, v191, v40, vcc
	v_mul_f32_e32 v41, 0xbfb8aa3b, v42
	v_exp_f32_e32 v41, v41
	s_nop 0
	v_pk_add_f32 v[40:41], v[40:41], 1.0 op_sel_hi:[1,0]
	s_nop 0
	v_rcp_f32_e32 v43, v41
	s_nop 3
	v_mul_f32_e32 v41, v42, v43
	s_nop 1
	v_rcp_f32_e32 v42, v40
	s_nop 3
	v_mul_f32_e32 v40, v37, v42
	s_nop 1
	v_pk_mul_f32 v[28:29], v[40:41], v[28:29]
	s_nop 0
	v_cvt_pk_bf16_f32 v27, v28, v29
	global_store_dwordx2 v[30:31], v[26:27], off offset:64
	global_load_dwordx2 v[38:39], v[46:47], off offset:3168
	s_nop 0
	global_load_dwordx4 v[26:29], v[62:63], off offset:192
	s_waitcnt vmcnt(1)
	v_lshlrev_b32_e32 v37, 16, v38
	v_mul_f32_e32 v40, 0xbfb8aa3b, v37
	v_fma_f32 v41, v37, s91, -v40
	v_rndne_f32_e32 v42, v40
	v_fmac_f32_e32 v41, 0xb2a5705f, v37
	v_sub_f32_e32 v40, v40, v42
	v_add_f32_e32 v40, v40, v41
	v_exp_f32_e32 v40, v40
	v_cvt_i32_f32_e32 v41, v42
	v_and_b32_e32 v38, 0xffff0000, v38
	v_cmp_nlt_f32_e32 vcc, s89, v37
	v_pk_mul_f32 v[34:35], v[34:35], v[36:37] op_sel_hi:[1,0]
	v_ldexp_f32 v40, v40, v41
	v_mul_f32_e32 v41, 0xbfb8aa3b, v38
	v_fma_f32 v42, v38, s91, -v41
	v_rndne_f32_e32 v43, v41
	v_fmac_f32_e32 v42, 0xb2a5705f, v38
	v_sub_f32_e32 v41, v41, v43
	v_add_f32_e32 v41, v41, v42
	v_exp_f32_e32 v41, v41
	v_cvt_i32_f32_e32 v42, v43
	v_cndmask_b32_e32 v40, 0, v40, vcc
	v_cmp_ngt_f32_e32 vcc, s88, v37
	s_waitcnt vmcnt(0)
	v_pk_mul_f32 v[26:27], v[26:27], v[34:35]
	v_ldexp_f32 v41, v41, v42
	v_cndmask_b32_e32 v40, v191, v40, vcc
	v_cmp_nlt_f32_e32 vcc, s89, v38
	s_nop 1
	v_cndmask_b32_e32 v41, 0, v41, vcc
	v_cmp_ngt_f32_e32 vcc, s88, v38
	s_nop 1
	v_cndmask_b32_e32 v41, v191, v41, vcc
	v_pk_add_f32 v[40:41], v[40:41], 1.0 op_sel_hi:[1,0]
	s_nop 0
	v_rcp_f32_e32 v42, v41
	s_nop 3
	v_mul_f32_e32 v41, v38, v42
	s_nop 1
	v_rcp_f32_e32 v38, v40
	s_nop 3
	v_mul_f32_e32 v40, v37, v38
	s_nop 1
	v_lshlrev_b32_e32 v37, 16, v39
	v_and_b32_e32 v38, 0xffff0000, v39
	v_pk_mul_f32 v[26:27], v[40:41], v[26:27]
	v_pk_mul_f32 v[32:33], v[32:33], v[36:37] op_sel_hi:[1,0]
	v_pk_mul_f32 v[28:29], v[28:29], v[32:33]
	v_mul_f32_e32 v34, 0xbfb8aa3b, v37
	v_exp_f32_e32 v34, v34
	s_nop 0
	v_cvt_pk_bf16_f32 v26, v26, v27
	v_mul_f32_e32 v35, 0xbfb8aa3b, v38
	v_exp_f32_e32 v35, v35
	s_nop 0
	v_pk_add_f32 v[34:35], v[34:35], 1.0 op_sel_hi:[1,0]
	s_nop 0
	v_rcp_f32_e32 v39, v35
	s_nop 3
	v_mul_f32_e32 v35, v38, v39
	s_nop 1
	v_rcp_f32_e32 v38, v34
	s_nop 3
	v_mul_f32_e32 v34, v37, v38
	s_nop 1
	v_pk_mul_f32 v[28:29], v[34:35], v[28:29]
	s_andn2_b64 vcc, exec, s[84:85]
	v_cvt_pk_bf16_f32 v27, v28, v29
	global_store_dwordx2 v[30:31], v[26:27], off offset:96
	s_cbranch_vccz .LBB0_1286

.LBB0_3593:
	ds_read_b128 v[30:33], v183
	ds_read_b128 v[26:29], v183 offset:64
	ds_read_b128 v[34:37], v184 offset:18432
	ds_read_b128 v[38:41], v184 offset:18496
	s_lshl_b32 s0, s93, 5
	s_sub_i32 s2, s86, s0
	s_lshr_b32 s0, s92, 24
	s_waitcnt lgkmcnt(1)
	v_mfma_f32_16x16x32_bf16 v[34:37], v[34:37], v[30:33], 0
	s_add_i32 s0, s86, s0
	s_ashr_i32 s0, s0, 8
	s_ashr_i32 s1, s0, 31
	s_waitcnt lgkmcnt(0)
	v_mfma_f32_16x16x32_bf16 v[54:57], v[38:41], v[26:29], v[34:37]
	ds_read_b128 v[38:41], v184 offset:20800
	s_ashr_i32 s3, s2, 31
	s_nop 0
	ds_read_b128 v[34:37], v184 offset:20736
	s_lshl_b64 s[0:1], s[0:1], 12
	s_lshl_b64 s[92:93], s[2:3], 7
	s_add_u32 s0, s0, s92
	s_addc_u32 s1, s1, s93
	s_waitcnt lgkmcnt(0)
	v_mfma_f32_16x16x32_bf16 v[34:37], v[34:37], v[30:33], 0
	s_lshl_b32 s86, s97, 7
	ds_read_b128 v[58:61], v184 offset:34624
	v_mfma_f32_16x16x32_bf16 v[62:65], v[38:41], v[26:29], v[34:37]
	ds_read_b128 v[38:41], v184 offset:23104
	s_nop 3
	ds_read_b128 v[34:37], v184 offset:23040
	s_waitcnt lgkmcnt(0)
	v_mfma_f32_16x16x32_bf16 v[34:37], v[34:37], v[30:33], 0
	v_mfma_f32_16x16x32_bf16 v[66:69], v[38:41], v[26:29], v[34:37]
	ds_read_b128 v[38:41], v184 offset:25408
	s_nop 5
	ds_read_b128 v[34:37], v184 offset:25344
	s_waitcnt lgkmcnt(0)
	v_mfma_f32_16x16x32_bf16 v[34:37], v[34:37], v[30:33], 0
	v_mfma_f32_16x16x32_bf16 v[50:53], v[38:41], v[26:29], v[34:37]
	ds_read_b128 v[38:41], v184 offset:27712
	s_nop 5
	ds_read_b128 v[34:37], v184 offset:27648
	s_waitcnt lgkmcnt(0)
	v_mfma_f32_16x16x32_bf16 v[34:37], v[34:37], v[30:33], 0
	v_mfma_f32_16x16x32_bf16 v[46:49], v[38:41], v[26:29], v[34:37]
	ds_read_b128 v[38:41], v184 offset:30016
	s_nop 5
	ds_read_b128 v[34:37], v184 offset:29952
	s_waitcnt lgkmcnt(0)
	v_mfma_f32_16x16x32_bf16 v[34:37], v[34:37], v[30:33], 0
	v_mfma_f32_16x16x32_bf16 v[42:45], v[38:41], v[26:29], v[34:37]
	ds_read_b128 v[38:41], v184 offset:32320
	s_nop 5
	ds_read_b128 v[34:37], v184 offset:32256
	s_waitcnt lgkmcnt(0)
	v_mfma_f32_16x16x32_bf16 v[34:37], v[34:37], v[30:33], 0
	v_mfma_f32_16x16x32_bf16 v[38:41], v[38:41], v[26:29], v[34:37]
	s_nop 6
	ds_read_b128 v[34:37], v184 offset:34560
	s_waitcnt lgkmcnt(0)
	v_mfma_f32_16x16x32_bf16 v[34:37], v[34:37], v[30:33], 0
	v_mfma_f32_16x16x32_bf16 v[34:37], v[58:61], v[26:29], v[34:37]
	v_mul_f32_e32 v58, v107, v89
	v_mul_f32_e32 v59, v108, v87
	v_cndmask_b32_e64 v58, v59, v58, s[6:7]
	v_mul_f32_e32 v59, v107, v91
	v_mul_f32_e32 v60, v108, v93
	v_cndmask_b32_e64 v59, v59, v60, s[12:13]
	v_mul_f32_e32 v58, 0x3fb8aa3b, v58
	v_mul_f32_e32 v59, 0x3fb8aa3b, v59
	v_exp_f32_e32 v58, v58
	v_exp_f32_e32 v59, v59
	v_mul_f32_e32 v60, v108, v120
	v_pk_mul_f32 v[58:59], v[58:59], v[54:55]
	v_mul_f32_e32 v54, v107, v119
	v_mul_f32_e32 v55, v108, v118
	v_cndmask_b32_e64 v54, v55, v54, s[14:15]
	v_mul_f32_e32 v55, v107, v121
	v_cndmask_b32_e64 v55, v60, v55, s[16:17]
	v_mul_f32_e32 v54, 0x3fb8aa3b, v54
	v_mul_f32_e32 v55, 0x3fb8aa3b, v55
	v_exp_f32_e32 v54, v54
	v_exp_f32_e32 v55, v55
	v_cvt_pk_bf16_f32 v58, v58, v59
	v_pk_mul_f32 v[60:61], v[54:55], v[56:57]
	v_mul_f32_e32 v54, v107, v123
	v_mul_f32_e32 v55, v108, v122
	v_cndmask_b32_e64 v54, v55, v54, s[18:19]
	v_mul_f32_e32 v55, v107, v125
	v_mul_f32_e32 v56, v108, v124
	v_cndmask_b32_e64 v55, v56, v55, s[20:21]
	v_mul_f32_e32 v54, 0x3fb8aa3b, v54
	v_mul_f32_e32 v55, 0x3fb8aa3b, v55
	v_exp_f32_e32 v54, v54
	v_exp_f32_e32 v55, v55
	v_mul_f32_e32 v56, v108, v128
	v_mul_f32_e32 v57, v108, v134
	v_cvt_pk_bf16_f32 v59, v60, v61
	v_pk_mul_f32 v[62:63], v[54:55], v[62:63]
	v_mul_f32_e32 v54, v107, v127
	v_mul_f32_e32 v55, v108, v126
	v_cndmask_b32_e64 v54, v55, v54, s[22:23]
	v_mul_f32_e32 v55, v107, v129
	v_cndmask_b32_e64 v55, v56, v55, s[24:25]
	v_mul_f32_e32 v54, 0x3fb8aa3b, v54
	v_mul_f32_e32 v55, 0x3fb8aa3b, v55
	v_exp_f32_e32 v54, v54
	v_exp_f32_e32 v55, v55
	v_mul_f32_e32 v56, v108, v132
	v_cvt_pk_bf16_f32 v60, v62, v63
	v_pk_mul_f32 v[64:65], v[54:55], v[64:65]
	v_mul_f32_e32 v54, v107, v131
	v_mul_f32_e32 v55, v108, v130
	v_cndmask_b32_e64 v54, v55, v54, s[26:27]
	v_mul_f32_e32 v55, v107, v133
	v_cndmask_b32_e64 v55, v56, v55, s[28:29]
	v_mul_f32_e32 v54, 0x3fb8aa3b, v54
	v_mul_f32_e32 v55, 0x3fb8aa3b, v55
	v_exp_f32_e32 v54, v54
	v_exp_f32_e32 v55, v55
	v_mul_f32_e32 v56, v107, v135
	v_cndmask_b32_e64 v56, v57, v56, s[30:31]
	v_mul_f32_e32 v57, v107, v137
	v_pk_mul_f32 v[54:55], v[54:55], v[66:67]
	v_mul_f32_e32 v66, v108, v136
	v_cndmask_b32_e64 v57, v66, v57, s[34:35]
	v_mul_f32_e32 v56, 0x3fb8aa3b, v56
	v_mul_f32_e32 v57, 0x3fb8aa3b, v57
	v_exp_f32_e32 v56, v56
	v_exp_f32_e32 v57, v57
	v_mul_f32_e32 v66, v107, v139
	v_mul_f32_e32 v67, v108, v138
	v_cndmask_b32_e64 v66, v67, v66, s[36:37]
	v_pk_mul_f32 v[56:57], v[56:57], v[68:69]
	v_mul_f32_e32 v67, v107, v141
	v_mul_f32_e32 v68, v108, v140
	v_cndmask_b32_e64 v67, v68, v67, s[38:39]
	v_mul_f32_e32 v66, 0x3fb8aa3b, v66
	v_mul_f32_e32 v67, 0x3fb8aa3b, v67
	v_exp_f32_e32 v66, v66
	v_exp_f32_e32 v67, v67
	v_mul_f32_e32 v68, v108, v144
	v_cvt_pk_bf16_f32 v61, v64, v65
	v_cvt_pk_bf16_f32 v54, v54, v55
	v_pk_mul_f32 v[50:51], v[66:67], v[50:51]
	v_mul_f32_e32 v66, v107, v143
	v_mul_f32_e32 v67, v108, v142
	v_cndmask_b32_e64 v66, v67, v66, s[40:41]
	v_mul_f32_e32 v67, v107, v145
	v_cndmask_b32_e64 v67, v68, v67, s[42:43]
	v_mul_f32_e32 v66, 0x3fb8aa3b, v66
	v_mul_f32_e32 v67, 0x3fb8aa3b, v67
	v_exp_f32_e32 v66, v66
	v_exp_f32_e32 v67, v67
	v_mul_f32_e32 v68, v108, v148
	v_cvt_pk_bf16_f32 v55, v56, v57
	v_cvt_pk_bf16_f32 v56, v50, v51
	v_pk_mul_f32 v[52:53], v[66:67], v[52:53]
	v_mul_f32_e32 v66, v107, v147
	v_mul_f32_e32 v67, v108, v146
	v_cndmask_b32_e64 v66, v67, v66, s[44:45]
	v_mul_f32_e32 v67, v107, v149
	v_cndmask_b32_e64 v67, v68, v67, s[46:47]
	v_mul_f32_e32 v66, 0x3fb8aa3b, v66
	v_mul_f32_e32 v67, 0x3fb8aa3b, v67
	v_exp_f32_e32 v66, v66
	v_exp_f32_e32 v67, v67
	v_mul_f32_e32 v68, v108, v152
	v_cvt_pk_bf16_f32 v57, v52, v53
	v_pk_mul_f32 v[46:47], v[66:67], v[46:47]
	v_mul_f32_e32 v66, v107, v151
	v_mul_f32_e32 v67, v108, v150
	v_cndmask_b32_e64 v66, v67, v66, s[48:49]
	v_mul_f32_e32 v67, v107, v153
	v_cndmask_b32_e64 v67, v68, v67, s[50:51]
	v_mul_f32_e32 v66, 0x3fb8aa3b, v66
	v_mul_f32_e32 v67, 0x3fb8aa3b, v67
	v_exp_f32_e32 v66, v66
	v_exp_f32_e32 v67, v67
	v_mul_f32_e32 v68, v108, v156
	v_cvt_pk_bf16_f32 v46, v46, v47
	v_pk_mul_f32 v[48:49], v[66:67], v[48:49]
	v_mul_f32_e32 v66, v107, v155
	v_mul_f32_e32 v67, v108, v154
	v_cndmask_b32_e64 v66, v67, v66, s[52:53]
	v_mul_f32_e32 v67, v107, v157
	v_cndmask_b32_e64 v67, v68, v67, s[54:55]
	v_mul_f32_e32 v66, 0x3fb8aa3b, v66
	v_mul_f32_e32 v67, 0x3fb8aa3b, v67
	v_exp_f32_e32 v66, v66
	v_exp_f32_e32 v67, v67
	v_mul_f32_e32 v68, v108, v160
	v_cvt_pk_bf16_f32 v47, v48, v49
	v_pk_mul_f32 v[42:43], v[66:67], v[42:43]
	v_mul_f32_e32 v66, v107, v159
	v_mul_f32_e32 v67, v108, v158
	v_cndmask_b32_e64 v66, v67, v66, s[56:57]
	v_mul_f32_e32 v67, v107, v161
	v_cndmask_b32_e64 v67, v68, v67, s[58:59]
	v_mul_f32_e32 v66, 0x3fb8aa3b, v66
	v_mul_f32_e32 v67, 0x3fb8aa3b, v67
	v_exp_f32_e32 v66, v66
	v_exp_f32_e32 v67, v67
	v_mul_f32_e32 v68, v108, v164
	v_cvt_pk_bf16_f32 v48, v42, v43
	v_pk_mul_f32 v[44:45], v[66:67], v[44:45]
	v_mul_f32_e32 v66, v107, v163
	v_mul_f32_e32 v67, v108, v162
	v_cndmask_b32_e64 v66, v67, v66, s[60:61]
	v_mul_f32_e32 v67, v107, v165
	v_cndmask_b32_e64 v67, v68, v67, s[62:63]
	v_mul_f32_e32 v66, 0x3fb8aa3b, v66
	v_mul_f32_e32 v67, 0x3fb8aa3b, v67
	v_exp_f32_e32 v66, v66
	v_exp_f32_e32 v67, v67
	v_mul_f32_e32 v68, v108, v168
	v_cvt_pk_bf16_f32 v49, v44, v45
	v_pk_mul_f32 v[38:39], v[66:67], v[38:39]
	v_mul_f32_e32 v66, v107, v167
	v_mul_f32_e32 v67, v108, v166
	v_cndmask_b32_e64 v66, v67, v66, s[64:65]
	v_mul_f32_e32 v67, v107, v169
	v_cndmask_b32_e64 v67, v68, v67, s[66:67]
	v_mul_f32_e32 v66, 0x3fb8aa3b, v66
	v_mul_f32_e32 v67, 0x3fb8aa3b, v67
	v_exp_f32_e32 v66, v66
	v_exp_f32_e32 v67, v67
	v_mul_f32_e32 v68, v108, v172
	v_cvt_pk_bf16_f32 v38, v38, v39
	v_pk_mul_f32 v[40:41], v[66:67], v[40:41]
	v_mul_f32_e32 v66, v107, v171
	v_mul_f32_e32 v67, v108, v170
	v_cndmask_b32_e64 v66, v67, v66, s[68:69]
	v_mul_f32_e32 v67, v107, v173
	v_cndmask_b32_e64 v67, v68, v67, s[70:71]
	v_mul_f32_e32 v66, 0x3fb8aa3b, v66
	v_mul_f32_e32 v67, 0x3fb8aa3b, v67
	v_exp_f32_e32 v66, v66
	v_exp_f32_e32 v67, v67
	v_mul_f32_e32 v68, v108, v176
	v_cvt_pk_bf16_f32 v39, v40, v41
	v_pk_mul_f32 v[34:35], v[66:67], v[34:35]
	v_mul_f32_e32 v66, v107, v175
	v_mul_f32_e32 v67, v108, v174
	v_cndmask_b32_e64 v66, v67, v66, s[72:73]
	v_mul_f32_e32 v67, v107, v177
	v_cndmask_b32_e64 v67, v68, v67, s[74:75]
	v_mul_f32_e32 v66, 0x3fb8aa3b, v66
	v_mul_f32_e32 v67, 0x3fb8aa3b, v67
	v_exp_f32_e32 v66, v66
	v_exp_f32_e32 v67, v67
	v_cvt_pk_bf16_f32 v40, v34, v35
	v_pk_mul_f32 v[36:37], v[66:67], v[36:37]
	ds_read_b64_tr_b16 v[64:65], v185 offset:39168
	ds_read_b64_tr_b16 v[62:63], v185 offset:36864
	ds_read_b64_tr_b16 v[66:67], v185 offset:36896
	ds_read_b64_tr_b16 v[68:69], v185 offset:39200
	ds_read_b64_tr_b16 v[110:111], v185 offset:36928
	ds_read_b64_tr_b16 v[112:113], v185 offset:39232
	ds_read_b64_tr_b16 v[192:193], v185 offset:36960
	ds_read_b64_tr_b16 v[194:195], v185 offset:39264
	s_waitcnt lgkmcnt(6)
	v_mfma_f32_16x16x32_bf16 v[62:65], v[62:65], v[58:61], 0
	v_cvt_pk_bf16_f32 v41, v36, v37
	s_waitcnt lgkmcnt(4)
	v_mfma_f32_16x16x32_bf16 v[66:69], v[66:69], v[58:61], 0
	s_waitcnt lgkmcnt(2)
	v_mfma_f32_16x16x32_bf16 v[110:113], v[110:113], v[58:61], 0
	s_waitcnt lgkmcnt(0)
	v_mfma_f32_16x16x32_bf16 v[58:61], v[192:195], v[58:61], 0
	ds_read_b64_tr_b16 v[52:53], v186 offset:39168
	ds_read_b64_tr_b16 v[50:51], v186 offset:36864
	ds_read_b64_tr_b16 v[192:193], v186 offset:36896
	ds_read_b64_tr_b16 v[194:195], v186 offset:39200
	s_waitcnt lgkmcnt(2)
	v_mfma_f32_16x16x32_bf16 v[50:53], v[50:53], v[54:57], v[62:65]
	s_waitcnt lgkmcnt(0)
	v_mfma_f32_16x16x32_bf16 v[62:65], v[192:195], v[54:57], v[66:69]
	s_nop 2
	ds_read_b64_tr_b16 v[66:67], v186 offset:36928
	ds_read_b64_tr_b16 v[68:69], v186 offset:39232
	s_waitcnt lgkmcnt(0)
	v_mfma_f32_16x16x32_bf16 v[66:69], v[66:69], v[54:57], v[110:113]
	s_nop 2
	ds_read_b64_tr_b16 v[110:111], v186 offset:36960
	ds_read_b64_tr_b16 v[112:113], v186 offset:39264
	s_waitcnt lgkmcnt(0)
	v_mfma_f32_16x16x32_bf16 v[54:57], v[110:113], v[54:57], v[58:61]
	ds_read_b64_tr_b16 v[44:45], v187 offset:39168
	ds_read_b64_tr_b16 v[42:43], v187 offset:36864
	s_nop 0
	ds_read_b64_tr_b16 v[58:59], v187 offset:36896
	ds_read_b64_tr_b16 v[60:61], v187 offset:39200
	s_waitcnt lgkmcnt(2)
	v_mfma_f32_16x16x32_bf16 v[42:45], v[42:45], v[46:49], v[50:53]
	s_nop 2
	ds_read_b64_tr_b16 v[50:51], v187 offset:36928
	ds_read_b64_tr_b16 v[52:53], v187 offset:39232
	s_waitcnt lgkmcnt(2)
	v_mfma_f32_16x16x32_bf16 v[58:61], v[58:61], v[46:49], v[62:65]
	s_waitcnt lgkmcnt(0)
	v_mfma_f32_16x16x32_bf16 v[62:65], v[50:53], v[46:49], v[66:69]
	ds_read_b64_tr_b16 v[50:51], v187 offset:36960
	ds_read_b64_tr_b16 v[52:53], v187 offset:39264
	s_waitcnt lgkmcnt(0)
	v_mfma_f32_16x16x32_bf16 v[54:57], v[50:53], v[46:49], v[54:57]
	ds_read_b64_tr_b16 v[36:37], v188 offset:39168
	ds_read_b64_tr_b16 v[34:35], v188 offset:36864
	ds_read_b64_tr_b16 v[46:47], v188 offset:36896
	ds_read_b64_tr_b16 v[48:49], v188 offset:39200
	s_waitcnt lgkmcnt(2)
	v_mfma_f32_16x16x32_bf16 v[50:53], v[34:37], v[38:41], v[42:45]
	s_nop 2
	ds_read_b64_tr_b16 v[42:43], v188 offset:36928
	ds_read_b64_tr_b16 v[44:45], v188 offset:39232
	s_waitcnt lgkmcnt(2)
	v_mfma_f32_16x16x32_bf16 v[34:37], v[46:49], v[38:41], v[58:61]
	s_waitcnt lgkmcnt(0)
	v_mfma_f32_16x16x32_bf16 v[46:49], v[42:45], v[38:41], v[62:65]
	ds_read_b64_tr_b16 v[42:43], v188 offset:36960
	ds_read_b64_tr_b16 v[44:45], v188 offset:39264
	ds_read_b128 v[110:113], v178 offset:59968
	ds_read_b128 v[62:65], v178 offset:57664
	s_waitcnt lgkmcnt(2)
	v_mfma_f32_16x16x32_bf16 v[192:195], v[42:45], v[38:41], v[54:57]
	ds_read_b128 v[38:41], v178 offset:55296
	s_nop 1
	ds_read_b128 v[54:57], v178 offset:55360
	ds_read_b128 v[42:45], v178 offset:64512
	s_waitcnt lgkmcnt(2)
	v_mfma_f32_16x16x32_bf16 v[38:41], v[38:41], v[30:33], 0
	ds_read_b128 v[66:69], v180 offset:64512
	ds_read_b128 v[196:199], v181 offset:64512
	s_waitcnt lgkmcnt(3)
	v_mfma_f32_16x16x32_bf16 v[54:57], v[54:57], v[26:29], v[38:41]
	s_nop 3
	ds_read_b128 v[38:41], v178 offset:64576
	s_waitcnt lgkmcnt(3)
	v_mfma_f32_16x16x32_bf16 v[42:45], v[42:45], v[30:33], 0
	s_waitcnt lgkmcnt(0)
	v_mfma_f32_16x16x32_bf16 v[58:61], v[38:41], v[26:29], v[42:45]
	ds_read_b128 v[38:41], v178 offset:57600
	s_nop 4
	ds_read_b128 v[42:45], v179 offset:64512
	s_waitcnt lgkmcnt(1)
	v_mfma_f32_16x16x32_bf16 v[38:41], v[38:41], v[30:33], 0
	v_mfma_f32_16x16x32_bf16 v[38:41], v[62:65], v[26:29], v[38:41]
	ds_read_b128 v[62:65], v179 offset:64576
	s_waitcnt lgkmcnt(1)
	v_mfma_f32_16x16x32_bf16 v[42:45], v[42:45], v[30:33], 0
	s_waitcnt lgkmcnt(0)
	v_mfma_f32_16x16x32_bf16 v[42:45], v[62:65], v[26:29], v[42:45]
	ds_read_b128 v[62:65], v178 offset:59904
	s_waitcnt lgkmcnt(0)
	v_mfma_f32_16x16x32_bf16 v[62:65], v[62:65], v[30:33], 0
	v_mfma_f32_16x16x32_bf16 v[62:65], v[110:113], v[26:29], v[62:65]
	ds_read_b128 v[110:113], v180 offset:64576
	v_mfma_f32_16x16x32_bf16 v[66:69], v[66:69], v[30:33], 0
	s_waitcnt lgkmcnt(0)
	v_mfma_f32_16x16x32_bf16 v[66:69], v[110:113], v[26:29], v[66:69]
	ds_read_b128 v[110:113], v178 offset:62208
	s_waitcnt lgkmcnt(0)
	v_mfma_f32_16x16x32_bf16 v[110:113], v[110:113], v[30:33], 0
	v_mfma_f32_16x16x32_bf16 v[30:33], v[196:199], v[30:33], 0
	ds_read_b128 v[196:199], v178 offset:62272
	s_waitcnt lgkmcnt(0)
	v_mfma_f32_16x16x32_bf16 v[196:199], v[196:199], v[26:29], v[110:113]
	s_nop 3
	ds_read_b128 v[110:113], v181 offset:64576
	s_waitcnt lgkmcnt(0)
	v_mfma_f32_16x16x32_bf16 v[26:29], v[110:113], v[26:29], v[30:33]
	s_nop 2
	v_mul_f32_e32 v30, v108, v1
	v_mul_f32_e32 v30, 0x3fb8aa3b, v30
	v_exp_f32_e32 v110, v30
	v_mul_f32_e32 v30, v107, v71
	v_mul_f32_e32 v30, 0x3fb8aa3b, v30
	v_exp_f32_e32 v112, v30
	s_nop 0
	v_pk_mul_f32 v[26:27], v[112:113], v[26:27] op_sel_hi:[0,1]
	v_pk_fma_f32 v[26:27], v[110:111], v[196:197], v[26:27] op_sel_hi:[0,1,1]
	v_pk_add_f32 v[32:33], v[192:193], v[26:27]
	v_pk_mul_f32 v[26:27], v[112:113], v[28:29] op_sel_hi:[0,1]
	v_pk_fma_f32 v[26:27], v[110:111], v[198:199], v[26:27] op_sel_hi:[0,1,1]
	v_pk_add_f32 v[108:109], v[194:195], v[26:27]
	v_lshl_add_u64 v[26:27], s[0:1], 0, v[82:83]
	v_mov_b64_e32 v[28:29], s[84:85]
	v_mad_u64_u32 v[28:29], s[0:1], v26, s95, v[28:29]
	v_pk_mul_f32 v[30:31], v[112:113], v[66:67] op_sel_hi:[0,1]
	v_mad_i32_i24 v29, v27, s95, v29
	v_lshlrev_b64 v[26:27], 12, v[26:27]
	v_pk_fma_f32 v[30:31], v[110:111], v[62:63], v[30:31] op_sel_hi:[0,1,1]
	v_lshl_add_u64 v[28:29], v[28:29], 0, s[86:87]
	v_lshl_add_u64 v[26:27], s[80:81], 0, v[26:27]
	v_pk_add_f32 v[66:67], v[46:47], v[30:31]
	v_lshl_add_u64 v[46:47], v[28:29], 0, v[72:73]
	v_lshl_add_u64 v[26:27], v[26:27], 0, s[86:87]
	s_lshl_b32 s86, s97, 8
	v_lshl_add_u64 v[30:31], v[26:27], 0, v[72:73]
	v_lshl_add_u64 v[62:63], v[84:85], 0, s[86:87]
	global_load_dwordx2 v[114:115], v[46:47], off offset:3072
	global_load_dwordx4 v[26:29], v[62:63], off
	v_pk_mul_f32 v[60:61], v[112:113], v[60:61] op_sel_hi:[0,1]
	v_pk_fma_f32 v[56:57], v[110:111], v[56:57], v[60:61] op_sel_hi:[0,1,1]
	v_pk_add_f32 v[52:53], v[52:53], v[56:57]
	v_pk_mul_f32 v[56:57], v[112:113], v[58:59] op_sel_hi:[0,1]
	v_pk_fma_f32 v[54:55], v[110:111], v[54:55], v[56:57] op_sel_hi:[0,1,1]
	v_pk_add_f32 v[54:55], v[50:51], v[54:55]
	v_pk_mul_f32 v[44:45], v[112:113], v[44:45] op_sel_hi:[0,1]
	v_add_f32_e32 v50, 0, v54
	v_add_f32_e32 v56, v55, v50
	v_add_f32_e32 v56, v52, v56
	s_mov_b32 s86, s96
	s_waitcnt vmcnt(1)
	v_lshlrev_b32_e32 v57, 16, v114
	v_and_b32_e32 v58, 0xffff0000, v114
	v_lshlrev_b32_e32 v60, 16, v115
	v_and_b32_e32 v61, 0xffff0000, v115
	v_mul_f32_e32 v50, 0xbfb8aa3b, v57
	v_exp_f32_e32 v50, v50
	s_nop 0
	v_mul_f32_e32 v51, 0xbfb8aa3b, v58
	v_exp_f32_e32 v51, v51
	s_nop 0
	v_pk_add_f32 v[50:51], v[50:51], 1.0 op_sel_hi:[1,0]
	s_nop 0
	v_rcp_f32_e32 v59, v51
	s_nop 3
	v_mul_f32_e32 v51, v58, v59
	s_nop 1
	v_div_scale_f32 v58, s[0:1], v50, v50, v57
	v_rcp_f32_e32 v59, v58
	v_pk_fma_f32 v[40:41], v[110:111], v[40:41], v[44:45] op_sel_hi:[0,1,1]
	v_pk_add_f32 v[36:37], v[36:37], v[40:41]
	v_pk_mul_f32 v[40:41], v[112:113], v[42:43] op_sel_hi:[0,1]
	v_fma_f32 v103, -v58, v59, 1.0
	v_fmac_f32_e32 v59, v103, v59
	v_div_scale_f32 v103, vcc, v57, v50, v57
	v_mul_f32_e32 v105, v103, v59
	v_fma_f32 v107, -v58, v105, v103
	v_fmac_f32_e32 v105, v107, v59
	v_fma_f32 v58, -v58, v105, v103
	v_div_fmas_f32 v58, v58, v59, v105
	v_div_fixup_f32 v50, v58, v50, v57
	v_add_f32_e32 v58, v53, v56
	v_pk_mul_f32 v[56:57], v[112:113], v[68:69] op_sel_hi:[0,1]
	v_pk_fma_f32 v[56:57], v[110:111], v[64:65], v[56:57] op_sel_hi:[0,1,1]
	v_pk_add_f32 v[56:57], v[48:49], v[56:57]
	v_pk_fma_f32 v[38:39], v[110:111], v[38:39], v[40:41] op_sel_hi:[0,1,1]
	v_pk_add_f32 v[34:35], v[34:35], v[38:39]
	v_add_f32_e32 v38, v58, v34
	v_mul_f32_e32 v48, 0xbfb8aa3b, v60
	v_exp_f32_e32 v48, v48
	s_nop 0
	v_add_f32_e32 v42, v35, v38
	v_mul_f32_e32 v49, 0xbfb8aa3b, v61
	v_exp_f32_e32 v49, v49
	s_nop 0
	v_pk_add_f32 v[48:49], v[48:49], 1.0 op_sel_hi:[1,0]
	s_nop 0
	v_rcp_f32_e32 v59, v49
	s_nop 3
	v_mul_f32_e32 v49, v61, v59
	s_nop 1
	v_rcp_f32_e32 v59, v48
	s_nop 3
	v_mul_f32_e32 v48, v60, v59
	s_nop 1
	global_load_dwordx2 v[60:61], v[46:47], off offset:3104
	s_waitcnt vmcnt(0)
	v_lshlrev_b32_e32 v40, 16, v60
	v_and_b32_e32 v41, 0xffff0000, v60
	v_lshlrev_b32_e32 v65, 16, v61
	v_and_b32_e32 v103, 0xffff0000, v61
	v_mul_f32_e32 v38, 0xbfb8aa3b, v40
	v_exp_f32_e32 v38, v38
	s_nop 0
	v_mul_f32_e32 v39, 0xbfb8aa3b, v41
	v_exp_f32_e32 v39, v39
	s_nop 0
	v_pk_add_f32 v[38:39], v[38:39], 1.0 op_sel_hi:[1,0]
	s_nop 0
	v_rcp_f32_e32 v43, v39
	s_nop 3
	v_mul_f32_e32 v41, v41, v43
	s_nop 1
	v_rcp_f32_e32 v39, v38
	s_nop 3
	v_mul_f32_e32 v40, v40, v39
	s_nop 1
	v_add_f32_e32 v38, v36, v42
	v_add_f32_e32 v38, v37, v38
	v_add_f32_e32 v38, v38, v66
	v_add_f32_e32 v38, v67, v38
	v_add_f32_e32 v38, v56, v38
	v_add_f32_e32 v38, v57, v38
	v_add_f32_e32 v38, v38, v32
	v_add_f32_e32 v38, v33, v38
	v_add_f32_e32 v38, v108, v38
	v_add_f32_e32 v38, v109, v38
	ds_bpermute_b32 v39, v116, v38
	v_cmp_nlt_f32_e32 vcc, s9, v65
	s_waitcnt lgkmcnt(0)
	v_add_f32_e32 v38, v38, v39
	ds_bpermute_b32 v39, v117, v38
	s_waitcnt lgkmcnt(0)
	v_add_f32_e32 v38, v38, v39
	v_mul_f32_e32 v64, 0x3c800000, v38
	v_pk_add_f32 v[38:39], v[56:57], v[64:65] op_sel_hi:[1,0] neg_lo:[0,1] neg_hi:[0,1]
	v_mul_f32_e32 v56, 0xbfb8aa3b, v65
	v_fma_f32 v57, v65, s8, -v56
	v_rndne_f32_e32 v105, v56
	v_fmac_f32_e32 v57, 0xb2a5705f, v65
	v_sub_f32_e32 v56, v56, v105
	v_add_f32_e32 v56, v56, v57
	v_exp_f32_e32 v56, v56
	v_cvt_i32_f32_e32 v57, v105
	v_pk_add_f32 v[44:45], v[34:35], v[64:65] op_sel_hi:[1,0] neg_lo:[0,1] neg_hi:[0,1]
	v_pk_add_f32 v[34:35], v[32:33], v[64:65] op_sel_hi:[1,0] neg_lo:[0,1] neg_hi:[0,1]
	v_pk_add_f32 v[32:33], v[108:109], v[64:65] op_sel_hi:[1,0] neg_lo:[0,1] neg_hi:[0,1]
	v_ldexp_f32 v56, v56, v57
	v_cndmask_b32_e32 v56, 0, v56, vcc
	v_cmp_ngt_f32_e32 vcc, s10, v65
	s_nop 1
	v_pk_add_f32 v[54:55], v[54:55], v[64:65] op_sel_hi:[1,0] neg_lo:[0,1] neg_hi:[0,1]
	v_cndmask_b32_e32 v56, v191, v56, vcc
	v_pk_mul_f32 v[68:69], v[54:55], v[54:55]
	v_pk_add_f32 v[52:53], v[52:53], v[64:65] op_sel_hi:[1,0] neg_lo:[0,1] neg_hi:[0,1]
	v_pk_mul_f32 v[110:111], v[52:53], v[52:53]
	v_add_f32_e32 v68, v68, v69
	v_mul_f32_e32 v57, 0xbfb8aa3b, v103
	v_exp_f32_e32 v57, v57
	s_nop 0
	v_pk_add_f32 v[56:57], v[56:57], 1.0 op_sel_hi:[1,0]
	v_add_f32_e32 v68, v110, v68
	v_div_scale_f32 v105, s[0:1], v57, v57, v103
	v_rcp_f32_e32 v107, v105
	v_pk_mul_f32 v[112:113], v[44:45], v[44:45]
	v_add_f32_e32 v68, v111, v68
	v_pk_add_f32 v[42:43], v[36:37], v[64:65] op_sel_hi:[1,0] neg_lo:[0,1] neg_hi:[0,1]
	v_fma_f32 v108, -v105, v107, 1.0
	v_fmac_f32_e32 v107, v108, v107
	v_div_scale_f32 v108, vcc, v103, v57, v103
	v_mul_f32_e32 v109, v108, v107
	v_fma_f32 v192, -v105, v109, v108
	v_fmac_f32_e32 v109, v192, v107
	v_fma_f32 v105, -v105, v109, v108
	v_div_fmas_f32 v105, v105, v107, v109
	v_div_fixup_f32 v57, v105, v57, v103
	v_div_scale_f32 v103, s[0:1], v56, v56, v65
	v_rcp_f32_e32 v105, v103
	v_add_f32_e32 v68, v112, v68
	v_pk_mul_f32 v[114:115], v[42:43], v[42:43]
	v_add_f32_e32 v68, v113, v68
	v_fma_f32 v107, -v103, v105, 1.0
	v_fmac_f32_e32 v105, v107, v105
	v_div_scale_f32 v107, vcc, v65, v56, v65
	v_mul_f32_e32 v108, v107, v105
	v_fma_f32 v109, -v103, v108, v107
	v_fmac_f32_e32 v108, v109, v105
	v_fma_f32 v103, -v103, v108, v107
	v_div_fmas_f32 v103, v103, v105, v108
	v_div_fixup_f32 v56, v103, v56, v65
	v_pk_add_f32 v[64:65], v[66:67], v[64:65] op_sel_hi:[1,0] neg_lo:[0,1] neg_hi:[0,1]
	v_add_f32_e32 v68, v114, v68
	v_pk_mul_f32 v[66:67], v[64:65], v[64:65]
	v_add_f32_e32 v68, v115, v68
	v_add_f32_e32 v66, v66, v68
	v_pk_mul_f32 v[36:37], v[38:39], v[38:39]
	v_add_f32_e32 v66, v67, v66
	v_add_f32_e32 v36, v36, v66
	v_pk_mul_f32 v[58:59], v[34:35], v[34:35]
	v_add_f32_e32 v36, v37, v36
	v_add_f32_e32 v36, v58, v36
	v_pk_mul_f32 v[60:61], v[32:33], v[32:33]
	v_add_f32_e32 v36, v59, v36
	v_add_f32_e32 v36, v60, v36
	v_add_f32_e32 v36, v61, v36
	ds_bpermute_b32 v37, v116, v36
	s_mov_b32 s0, 0xf800000
	global_load_dwordx2 v[108:109], v[46:47], off offset:3136
	s_waitcnt lgkmcnt(0)
	v_add_f32_e32 v36, v36, v37
	ds_bpermute_b32 v37, v117, v36
	s_waitcnt lgkmcnt(0)
	v_add_f32_e32 v36, v36, v37
	v_fmamk_f32 v36, v36, 0x3c800000, v189
	v_cmp_gt_f32_e32 vcc, s0, v36
	v_mul_f32_e32 v37, 0x4f800000, v36
	s_nop 0
	v_cndmask_b32_e32 v36, v36, v37, vcc
	v_sqrt_f32_e32 v37, v36
	s_nop 0
	v_add_u32_e32 v58, -1, v37
	v_fma_f32 v59, -v58, v37, v36
	v_cmp_ge_f32_e64 s[0:1], 0, v59
	v_add_u32_e32 v59, 1, v37
	s_nop 0
	v_cndmask_b32_e64 v58, v37, v58, s[0:1]
	v_fma_f32 v37, -v59, v37, v36
	v_cmp_lt_f32_e64 s[0:1], 0, v37
	s_nop 1
	v_cndmask_b32_e64 v37, v58, v59, s[0:1]
	v_mul_f32_e32 v58, 0x37800000, v37
	v_cndmask_b32_e32 v37, v37, v58, vcc
	v_cmp_class_f32_e32 vcc, v36, v190
	s_nop 1
	v_cndmask_b32_e32 v36, v37, v36, vcc
	v_rcp_f32_e32 v36, v36
	s_nop 3
	v_pk_mul_f32 v[54:55], v[54:55], v[36:37] op_sel_hi:[1,0]
	v_pk_mul_f32 v[44:45], v[44:45], v[36:37] op_sel_hi:[1,0]
	v_pk_mul_f32 v[26:27], v[26:27], v[54:55]
	s_nop 0
	v_pk_mul_f32 v[26:27], v[50:51], v[26:27]
	v_pk_mul_f32 v[50:51], v[52:53], v[36:37] op_sel_hi:[1,0]
	v_cvt_pk_bf16_f32 v26, v26, v27
	v_pk_mul_f32 v[28:29], v[28:29], v[50:51]
	s_nop 0
	v_pk_mul_f32 v[28:29], v[48:49], v[28:29]
	s_nop 0
	v_cvt_pk_bf16_f32 v27, v28, v29
	global_store_dwordx2 v[30:31], v[26:27], off
	global_load_dwordx4 v[26:29], v[62:63], off offset:64
	s_waitcnt vmcnt(0)
	v_pk_mul_f32 v[26:27], v[26:27], v[44:45]
	s_nop 0
	v_pk_mul_f32 v[26:27], v[40:41], v[26:27]
	v_pk_mul_f32 v[40:41], v[42:43], v[36:37] op_sel_hi:[1,0]
	v_cvt_pk_bf16_f32 v26, v26, v27
	v_pk_mul_f32 v[28:29], v[28:29], v[40:41]
	v_lshlrev_b32_e32 v37, 16, v108
	v_pk_mul_f32 v[28:29], v[56:57], v[28:29]
	v_mul_f32_e32 v40, 0xbfb8aa3b, v37
	v_cvt_pk_bf16_f32 v27, v28, v29
	global_store_dwordx2 v[30:31], v[26:27], off offset:32
	global_load_dwordx4 v[26:29], v[62:63], off offset:128
	v_fma_f32 v41, v37, s8, -v40
	v_rndne_f32_e32 v43, v40
	v_fmac_f32_e32 v41, 0xb2a5705f, v37
	v_sub_f32_e32 v40, v40, v43
	v_add_f32_e32 v40, v40, v41
	v_exp_f32_e32 v40, v40
	v_cvt_i32_f32_e32 v41, v43
	v_and_b32_e32 v42, 0xffff0000, v108
	v_cmp_nlt_f32_e32 vcc, s9, v37
	v_ldexp_f32 v40, v40, v41
	v_cndmask_b32_e32 v40, 0, v40, vcc
	v_cmp_ngt_f32_e32 vcc, s10, v37
	s_nop 1
	v_cndmask_b32_e32 v40, v191, v40, vcc
	v_mul_f32_e32 v41, 0xbfb8aa3b, v42
	v_exp_f32_e32 v41, v41
	s_nop 0
	v_pk_add_f32 v[40:41], v[40:41], 1.0 op_sel_hi:[1,0]
	s_nop 0
	v_rcp_f32_e32 v43, v41
	s_nop 3
	v_mul_f32_e32 v41, v42, v43
	s_nop 1
	v_rcp_f32_e32 v42, v40
	s_nop 3
	v_mul_f32_e32 v40, v37, v42
	s_nop 1
	v_pk_mul_f32 v[42:43], v[64:65], v[36:37] op_sel_hi:[1,0]
	v_lshlrev_b32_e32 v37, 16, v109
	v_cmp_nlt_f32_e32 vcc, s9, v37
	v_pk_mul_f32 v[38:39], v[38:39], v[36:37] op_sel_hi:[1,0]
	s_waitcnt vmcnt(0)
	v_pk_mul_f32 v[26:27], v[26:27], v[42:43]
	s_nop 0
	v_pk_mul_f32 v[26:27], v[40:41], v[26:27]
	v_mul_f32_e32 v40, 0xbfb8aa3b, v37
	v_fma_f32 v41, v37, s8, -v40
	v_rndne_f32_e32 v43, v40
	v_fmac_f32_e32 v41, 0xb2a5705f, v37
	v_sub_f32_e32 v40, v40, v43
	v_add_f32_e32 v40, v40, v41
	v_exp_f32_e32 v40, v40
	v_cvt_i32_f32_e32 v41, v43
	v_and_b32_e32 v42, 0xffff0000, v109
	v_pk_mul_f32 v[28:29], v[28:29], v[38:39]
	v_cvt_pk_bf16_f32 v26, v26, v27
	v_ldexp_f32 v40, v40, v41
	v_cndmask_b32_e32 v40, 0, v40, vcc
	v_cmp_ngt_f32_e32 vcc, s10, v37
	s_nop 1
	v_cndmask_b32_e32 v40, v191, v40, vcc
	v_mul_f32_e32 v41, 0xbfb8aa3b, v42
	v_exp_f32_e32 v41, v41
	s_nop 0
	v_pk_add_f32 v[40:41], v[40:41], 1.0 op_sel_hi:[1,0]
	s_nop 0
	v_rcp_f32_e32 v43, v41
	s_nop 3
	v_mul_f32_e32 v41, v42, v43
	s_nop 1
	v_rcp_f32_e32 v42, v40
	s_nop 3
	v_mul_f32_e32 v40, v37, v42
	s_nop 1
	v_pk_mul_f32 v[28:29], v[40:41], v[28:29]
	s_nop 0
	v_cvt_pk_bf16_f32 v27, v28, v29
	global_store_dwordx2 v[30:31], v[26:27], off offset:64
	global_load_dwordx2 v[38:39], v[46:47], off offset:3168
	s_nop 0
	global_load_dwordx4 v[26:29], v[62:63], off offset:192
	s_waitcnt vmcnt(1)
	v_lshlrev_b32_e32 v37, 16, v38
	v_mul_f32_e32 v40, 0xbfb8aa3b, v37
	v_fma_f32 v41, v37, s8, -v40
	v_rndne_f32_e32 v42, v40
	v_fmac_f32_e32 v41, 0xb2a5705f, v37
	v_sub_f32_e32 v40, v40, v42
	v_add_f32_e32 v40, v40, v41
	v_exp_f32_e32 v40, v40
	v_cvt_i32_f32_e32 v41, v42
	v_and_b32_e32 v38, 0xffff0000, v38
	v_cmp_nlt_f32_e32 vcc, s9, v37
	v_pk_mul_f32 v[34:35], v[34:35], v[36:37] op_sel_hi:[1,0]
	v_ldexp_f32 v40, v40, v41
	v_mul_f32_e32 v41, 0xbfb8aa3b, v38
	v_fma_f32 v42, v38, s8, -v41
	v_rndne_f32_e32 v43, v41
	v_fmac_f32_e32 v42, 0xb2a5705f, v38
	v_sub_f32_e32 v41, v41, v43
	v_add_f32_e32 v41, v41, v42
	v_exp_f32_e32 v41, v41
	v_cvt_i32_f32_e32 v42, v43
	v_cndmask_b32_e32 v40, 0, v40, vcc
	v_cmp_ngt_f32_e32 vcc, s10, v37
	s_waitcnt vmcnt(0)
	v_pk_mul_f32 v[26:27], v[26:27], v[34:35]
	v_ldexp_f32 v41, v41, v42
	v_cndmask_b32_e32 v40, v191, v40, vcc
	v_cmp_nlt_f32_e32 vcc, s9, v38
	s_nop 1
	v_cndmask_b32_e32 v41, 0, v41, vcc
	v_cmp_ngt_f32_e32 vcc, s10, v38
	s_nop 1
	v_cndmask_b32_e32 v41, v191, v41, vcc
	v_pk_add_f32 v[40:41], v[40:41], 1.0 op_sel_hi:[1,0]
	s_nop 0
	v_rcp_f32_e32 v42, v41
	s_nop 3
	v_mul_f32_e32 v41, v38, v42
	s_nop 1
	v_rcp_f32_e32 v38, v40
	s_nop 3
	v_mul_f32_e32 v40, v37, v38
	s_nop 1
	v_lshlrev_b32_e32 v37, 16, v39
	v_and_b32_e32 v38, 0xffff0000, v39
	v_pk_mul_f32 v[26:27], v[40:41], v[26:27]
	v_pk_mul_f32 v[32:33], v[32:33], v[36:37] op_sel_hi:[1,0]
	v_pk_mul_f32 v[28:29], v[28:29], v[32:33]
	v_mul_f32_e32 v34, 0xbfb8aa3b, v37
	v_exp_f32_e32 v34, v34
	s_nop 0
	v_cvt_pk_bf16_f32 v26, v26, v27
	v_mul_f32_e32 v35, 0xbfb8aa3b, v38
	v_exp_f32_e32 v35, v35
	s_nop 0
	v_pk_add_f32 v[34:35], v[34:35], 1.0 op_sel_hi:[1,0]
	s_nop 0
	v_rcp_f32_e32 v39, v35
	s_nop 3
	v_mul_f32_e32 v35, v38, v39
	s_nop 1
	v_rcp_f32_e32 v38, v34
	s_nop 3
	v_mul_f32_e32 v34, v37, v38
	s_nop 1
	v_pk_mul_f32 v[28:29], v[34:35], v[28:29]
	s_andn2_b64 vcc, exec, s[88:89]
	v_cvt_pk_bf16_f32 v27, v28, v29
	global_store_dwordx2 v[30:31], v[26:27], off offset:96
	s_cbranch_vccz .LBB0_3604
